# static priority raise (s_setprio 3) for the single wave that runs the grid-barrier protocol, back to 0 when the barrier is passed
# baseline (speedup 1.0000x reference)
; __device__ __forceinline__ unsigned xb_ld(unsigned* p)              { return __hip_atomic_load(p, __ATOMIC_RELAXED, __HIP_MEMORY_SCOPE_AGENT); }
; __device__ __forceinline__ unsigned xb_add(unsigned* p, unsigned v) { return __hip_atomic_fetch_add(p, v, __ATOMIC_RELAXED, __HIP_MEMORY_SCOPE_AGENT); }
; #define XB_SPIN(cond, bar) do { unsigned _sp = 0; while (cond) { __builtin_amdgcn_s_sleep(1); \
;     if ((++_sp & 255u) == 0u) { if (xb_ld(&(bar)[XB_TMO])) break; if (_sp > XB_SPIN_CAP) { atomicAdd(&(bar)[XB_TMO], 1u); break; } } } } while (0)
; __device__ __forceinline__ void xcd_barrier(const XcdBarrier& b) {
;   asm volatile("s_waitcnt vmcnt(0)" ::: "memory");
;   __syncthreads();
;   if (threadIdx.x == 0) {
;     unsigned* bar = b.bar;
;     __builtin_amdgcn_s_waitcnt(0);
;     unsigned nloc = b.st[0], nx = b.st[1];
;     if (nloc == 0u) { xcd_barrier_complete(bar, b.x, nloc, nx); b.st[0] = nloc; b.st[1] = nx; }
;     const unsigned old = xb_add(&bar[XB_XSUB(b.x)], 1u);
;     const unsigned gen = old / nloc;
;     if (old + 1u == (gen + 1u) * nloc) {
;       __builtin_amdgcn_fence(__ATOMIC_RELEASE, "agent");
;       asm volatile("s_waitcnt vmcnt(0)" ::: "memory");
;       const unsigned og = xb_add(&bar[XB_TOP], 1u);
;       const unsigned tg = og / nx;
;       if (og + 1u == (tg + 1u) * nx) xb_add(&bar[XB_TOPGEN], 1u);
;       else XB_SPIN(xb_ld(&bar[XB_TOPGEN]) == tg, bar);
;       __builtin_amdgcn_fence(__ATOMIC_ACQUIRE, "agent");
;       xb_add(&bar[XB_XGEN(b.x)], 1u);
.LBB0_72:
	s_waitcnt vmcnt(0) lgkmcnt(0)
	s_add_u32 s98, s98, 1
	s_setprio 3
	v_mov_b32_e32 v253, 0x12810
	ds_read_b32 v254, v253
	ds_read_b32 v253, v253 offset:4
	s_lshl_b32 s101, s33, 8
	s_add_u32 s99, s101, 5120
	s_waitcnt lgkmcnt(0)
	v_readfirstlane_b32 s100, v254
	v_mov_b32_e32 v254, s99
	v_readfirstlane_b32 s99, v253
	s_nop 0
	v_mov_b32_e32 v253, v254
	v_mov_b32_e32 v254, 1
	global_atomic_add v254, v253, v254, s[44:45] offset:64 sc0
	buffer_inv sc1
	s_mul_i32 s100, s100, s98
	s_mul_i32 s99, s99, s98
	s_waitcnt vmcnt(0)
	v_add_u32_e32 v254, 1, v254
	v_cmp_ne_u32_e32 vcc, s100, v254
	s_cbranch_vccnz .Lgb_wait_1
	buffer_wbl2 sc1
	s_waitcnt vmcnt(0)
	v_mov_b32_e32 v254, 1
	v_mov_b32_e32 v253, 9216
	global_atomic_add v253, v254, s[44:45] offset:64
	global_atomic_add v253, v254, s[44:45] offset:320
	global_atomic_add v253, v254, s[44:45] offset:576
	global_atomic_add v253, v254, s[44:45] offset:832
	global_atomic_add v253, v254, s[44:45] offset:1088
	global_atomic_add v253, v254, s[44:45] offset:1344
	global_atomic_add v253, v254, s[44:45] offset:1600
	global_atomic_add v253, v254, s[44:45] offset:1856
	v_mov_b32_e32 v253, 11264
	global_atomic_add v253, v254, s[44:45] offset:64
	global_atomic_add v253, v254, s[44:45] offset:320
	global_atomic_add v253, v254, s[44:45] offset:576
	global_atomic_add v253, v254, s[44:45] offset:832
	global_atomic_add v253, v254, s[44:45] offset:1088
	global_atomic_add v253, v254, s[44:45] offset:1344
	global_atomic_add v253, v254, s[44:45] offset:1600
	global_atomic_add v253, v254, s[44:45] offset:1856

; __device__ __forceinline__ unsigned xb_ld(unsigned* p)              { return __hip_atomic_load(p, __ATOMIC_RELAXED, __HIP_MEMORY_SCOPE_AGENT); }
; __device__ __forceinline__ unsigned xb_add(unsigned* p, unsigned v) { return __hip_atomic_fetch_add(p, v, __ATOMIC_RELAXED, __HIP_MEMORY_SCOPE_AGENT); }
; #define XB_SPIN(cond, bar) do { unsigned _sp = 0; while (cond) { __builtin_amdgcn_s_sleep(1); \
;     if ((++_sp & 255u) == 0u) { if (xb_ld(&(bar)[XB_TMO])) break; if (_sp > XB_SPIN_CAP) { atomicAdd(&(bar)[XB_TMO], 1u); break; } } } } while (0)
; __device__ __forceinline__ void xcd_barrier(const XcdBarrier& b) {
;     ...
;       else XB_SPIN(xb_ld(&bar[XB_TOPGEN]) == tg, bar);
;       __builtin_amdgcn_fence(__ATOMIC_ACQUIRE, "agent");
;       xb_add(&bar[XB_XGEN(b.x)], 1u);
.Lgb_wd_1:
	s_setprio 0

; __device__ __forceinline__ unsigned xb_ld(unsigned* p)              { return __hip_atomic_load(p, __ATOMIC_RELAXED, __HIP_MEMORY_SCOPE_AGENT); }
; __device__ __forceinline__ unsigned xb_add(unsigned* p, unsigned v) { return __hip_atomic_fetch_add(p, v, __ATOMIC_RELAXED, __HIP_MEMORY_SCOPE_AGENT); }
; #define XB_SPIN(cond, bar) do { unsigned _sp = 0; while (cond) { __builtin_amdgcn_s_sleep(1); \
;     if ((++_sp & 255u) == 0u) { if (xb_ld(&(bar)[XB_TMO])) break; if (_sp > XB_SPIN_CAP) { atomicAdd(&(bar)[XB_TMO], 1u); break; } } } } while (0)
; __device__ __forceinline__ void xcd_barrier(const XcdBarrier& b) {
;   asm volatile("s_waitcnt vmcnt(0)" ::: "memory");
;   __syncthreads();
;   if (threadIdx.x == 0) {
;     unsigned* bar = b.bar;
;     __builtin_amdgcn_s_waitcnt(0);
;     unsigned nloc = b.st[0], nx = b.st[1];
;     if (nloc == 0u) { xcd_barrier_complete(bar, b.x, nloc, nx); b.st[0] = nloc; b.st[1] = nx; }
;     const unsigned old = xb_add(&bar[XB_XSUB(b.x)], 1u);
;     const unsigned gen = old / nloc;
;     if (old + 1u == (gen + 1u) * nloc) {
;       __builtin_amdgcn_fence(__ATOMIC_RELEASE, "agent");
;       asm volatile("s_waitcnt vmcnt(0)" ::: "memory");
;       const unsigned og = xb_add(&bar[XB_TOP], 1u);
;       const unsigned tg = og / nx;
;       if (og + 1u == (tg + 1u) * nx) xb_add(&bar[XB_TOPGEN], 1u);
;       else XB_SPIN(xb_ld(&bar[XB_TOPGEN]) == tg, bar);
;       __builtin_amdgcn_fence(__ATOMIC_ACQUIRE, "agent");
;       xb_add(&bar[XB_XGEN(b.x)], 1u);
.LBB0_115:
	s_waitcnt vmcnt(0)
	s_barrier
	s_and_saveexec_b64 s[6:7], s[4:5]
	s_cbranch_execz .LBB0_167
	s_waitcnt vmcnt(0) lgkmcnt(0)
	s_add_u32 s98, s98, 1
	s_setprio 3
	v_mov_b32_e32 v253, 0x12810
	ds_read_b32 v254, v253
	ds_read_b32 v253, v253 offset:4
	s_lshl_b32 s101, s33, 8
	s_add_u32 s99, s101, 5120
	s_waitcnt lgkmcnt(0)
	v_readfirstlane_b32 s100, v254
	v_mov_b32_e32 v254, s99
	v_readfirstlane_b32 s99, v253
	s_nop 0
	v_mov_b32_e32 v253, v254
	v_mov_b32_e32 v254, 1
	global_atomic_add v254, v253, v254, s[44:45] offset:64 sc0
	buffer_inv sc1
	s_mul_i32 s100, s100, s98
	s_mul_i32 s99, s99, s98
	s_waitcnt vmcnt(0)
	v_add_u32_e32 v254, 1, v254
	v_cmp_ne_u32_e32 vcc, s100, v254
	s_cbranch_vccnz .Lgb_wait_2
	buffer_wbl2 sc1
	s_waitcnt vmcnt(0)
	v_mov_b32_e32 v254, 1
	v_mov_b32_e32 v253, 9216
	global_atomic_add v253, v254, s[44:45] offset:64
	global_atomic_add v253, v254, s[44:45] offset:320
	global_atomic_add v253, v254, s[44:45] offset:576
	global_atomic_add v253, v254, s[44:45] offset:832
	global_atomic_add v253, v254, s[44:45] offset:1088
	global_atomic_add v253, v254, s[44:45] offset:1344
	global_atomic_add v253, v254, s[44:45] offset:1600
	global_atomic_add v253, v254, s[44:45] offset:1856
	v_mov_b32_e32 v253, 11264
	global_atomic_add v253, v254, s[44:45] offset:64
	global_atomic_add v253, v254, s[44:45] offset:320
	global_atomic_add v253, v254, s[44:45] offset:576
	global_atomic_add v253, v254, s[44:45] offset:832
	global_atomic_add v253, v254, s[44:45] offset:1088
	global_atomic_add v253, v254, s[44:45] offset:1344
	global_atomic_add v253, v254, s[44:45] offset:1600
	global_atomic_add v253, v254, s[44:45] offset:1856

; __device__ __forceinline__ unsigned xb_ld(unsigned* p)              { return __hip_atomic_load(p, __ATOMIC_RELAXED, __HIP_MEMORY_SCOPE_AGENT); }
; __device__ __forceinline__ unsigned xb_add(unsigned* p, unsigned v) { return __hip_atomic_fetch_add(p, v, __ATOMIC_RELAXED, __HIP_MEMORY_SCOPE_AGENT); }
; #define XB_SPIN(cond, bar) do { unsigned _sp = 0; while (cond) { __builtin_amdgcn_s_sleep(1); \
;     if ((++_sp & 255u) == 0u) { if (xb_ld(&(bar)[XB_TMO])) break; if (_sp > XB_SPIN_CAP) { atomicAdd(&(bar)[XB_TMO], 1u); break; } } } } while (0)
; __device__ __forceinline__ void xcd_barrier(const XcdBarrier& b) {
;   asm volatile("s_waitcnt vmcnt(0)" ::: "memory");
;   __syncthreads();
;   if (threadIdx.x == 0) {
;     unsigned* bar = b.bar;
;     __builtin_amdgcn_s_waitcnt(0);
;     unsigned nloc = b.st[0], nx = b.st[1];
;     if (nloc == 0u) { xcd_barrier_complete(bar, b.x, nloc, nx); b.st[0] = nloc; b.st[1] = nx; }
;     const unsigned old = xb_add(&bar[XB_XSUB(b.x)], 1u);
;     const unsigned gen = old / nloc;
;     if (old + 1u == (gen + 1u) * nloc) {
;       __builtin_amdgcn_fence(__ATOMIC_RELEASE, "agent");
;       asm volatile("s_waitcnt vmcnt(0)" ::: "memory");
;       const unsigned og = xb_add(&bar[XB_TOP], 1u);
;       const unsigned tg = og / nx;
;       if (og + 1u == (tg + 1u) * nx) xb_add(&bar[XB_TOPGEN], 1u);
;       else XB_SPIN(xb_ld(&bar[XB_TOPGEN]) == tg, bar);
;       __builtin_amdgcn_fence(__ATOMIC_ACQUIRE, "agent");
;       xb_add(&bar[XB_XGEN(b.x)], 1u);
.LBB0_179:
	s_or_b64 exec, exec, s[10:11]
	s_waitcnt vmcnt(0)
	s_barrier
	s_and_saveexec_b64 s[6:7], s[4:5]
	s_cbranch_execz .LBB0_231
	s_waitcnt vmcnt(0) lgkmcnt(0)
	s_add_u32 s98, s98, 1
	s_setprio 3
	v_mov_b32_e32 v253, 0x12810
	ds_read_b32 v254, v253
	ds_read_b32 v253, v253 offset:4
	s_lshl_b32 s101, s33, 8
	s_add_u32 s99, s101, 5120
	s_waitcnt lgkmcnt(0)
	v_readfirstlane_b32 s100, v254
	v_mov_b32_e32 v254, s99
	v_readfirstlane_b32 s99, v253
	s_nop 0
	v_mov_b32_e32 v253, v254
	v_mov_b32_e32 v254, 1
	global_atomic_add v254, v253, v254, s[44:45] offset:64 sc0
	buffer_inv sc1
	s_mul_i32 s100, s100, s98
	s_mul_i32 s99, s99, s98
	s_waitcnt vmcnt(0)
	v_add_u32_e32 v254, 1, v254
	v_cmp_ne_u32_e32 vcc, s100, v254
	s_cbranch_vccnz .Lgb_wait_3
	buffer_wbl2 sc1
	s_waitcnt vmcnt(0)
	v_mov_b32_e32 v254, 1
	v_mov_b32_e32 v253, 9216
	global_atomic_add v253, v254, s[44:45] offset:64
	global_atomic_add v253, v254, s[44:45] offset:320
	global_atomic_add v253, v254, s[44:45] offset:576
	global_atomic_add v253, v254, s[44:45] offset:832
	global_atomic_add v253, v254, s[44:45] offset:1088
	global_atomic_add v253, v254, s[44:45] offset:1344
	global_atomic_add v253, v254, s[44:45] offset:1600
	global_atomic_add v253, v254, s[44:45] offset:1856
	v_mov_b32_e32 v253, 11264
	global_atomic_add v253, v254, s[44:45] offset:64
	global_atomic_add v253, v254, s[44:45] offset:320
	global_atomic_add v253, v254, s[44:45] offset:576
	global_atomic_add v253, v254, s[44:45] offset:832
	global_atomic_add v253, v254, s[44:45] offset:1088
	global_atomic_add v253, v254, s[44:45] offset:1344
	global_atomic_add v253, v254, s[44:45] offset:1600
	global_atomic_add v253, v254, s[44:45] offset:1856

; __device__ __forceinline__ unsigned xb_ld(unsigned* p)              { return __hip_atomic_load(p, __ATOMIC_RELAXED, __HIP_MEMORY_SCOPE_AGENT); }
; __device__ __forceinline__ unsigned xb_add(unsigned* p, unsigned v) { return __hip_atomic_fetch_add(p, v, __ATOMIC_RELAXED, __HIP_MEMORY_SCOPE_AGENT); }
; #define XB_SPIN(cond, bar) do { unsigned _sp = 0; while (cond) { __builtin_amdgcn_s_sleep(1); \
;     if ((++_sp & 255u) == 0u) { if (xb_ld(&(bar)[XB_TMO])) break; if (_sp > XB_SPIN_CAP) { atomicAdd(&(bar)[XB_TMO], 1u); break; } } } } while (0)
; __device__ __forceinline__ void xcd_barrier(const XcdBarrier& b) {
;   asm volatile("s_waitcnt vmcnt(0)" ::: "memory");
;   __syncthreads();
;   if (threadIdx.x == 0) {
;     unsigned* bar = b.bar;
;     __builtin_amdgcn_s_waitcnt(0);
;     unsigned nloc = b.st[0], nx = b.st[1];
;     if (nloc == 0u) { xcd_barrier_complete(bar, b.x, nloc, nx); b.st[0] = nloc; b.st[1] = nx; }
;     const unsigned old = xb_add(&bar[XB_XSUB(b.x)], 1u);
;     const unsigned gen = old / nloc;
;     if (old + 1u == (gen + 1u) * nloc) {
;       __builtin_amdgcn_fence(__ATOMIC_RELEASE, "agent");
;       asm volatile("s_waitcnt vmcnt(0)" ::: "memory");
;       const unsigned og = xb_add(&bar[XB_TOP], 1u);
;       const unsigned tg = og / nx;
;       if (og + 1u == (tg + 1u) * nx) xb_add(&bar[XB_TOPGEN], 1u);
;       else XB_SPIN(xb_ld(&bar[XB_TOPGEN]) == tg, bar);
;       __builtin_amdgcn_fence(__ATOMIC_ACQUIRE, "agent");
;       xb_add(&bar[XB_XGEN(b.x)], 1u);
.LBB0_572:
	s_waitcnt vmcnt(0)
	s_waitcnt lgkmcnt(0)
	s_barrier
	s_and_saveexec_b64 s[6:7], s[4:5]
	s_cbranch_execz .LBB0_624
	s_waitcnt vmcnt(0) lgkmcnt(0)
	s_add_u32 s98, s98, 1
	s_setprio 3
	v_mov_b32_e32 v253, 0x12810
	ds_read_b32 v254, v253
	ds_read_b32 v253, v253 offset:4
	s_lshl_b32 s101, s33, 8
	s_add_u32 s99, s101, 5120
	s_waitcnt lgkmcnt(0)
	v_readfirstlane_b32 s100, v254
	v_mov_b32_e32 v254, s99
	v_readfirstlane_b32 s99, v253
	s_nop 0
	v_mov_b32_e32 v253, v254
	v_mov_b32_e32 v254, 1
	global_atomic_add v254, v253, v254, s[44:45] offset:64 sc0
	buffer_inv sc1
	s_mul_i32 s100, s100, s98
	s_mul_i32 s99, s99, s98
	s_waitcnt vmcnt(0)
	v_add_u32_e32 v254, 1, v254
	v_cmp_ne_u32_e32 vcc, s100, v254
	s_cbranch_vccnz .Lgb_wait_4
	buffer_wbl2 sc1
	s_waitcnt vmcnt(0)
	v_mov_b32_e32 v254, 1
	v_mov_b32_e32 v253, 9216
	global_atomic_add v253, v254, s[44:45] offset:64
	global_atomic_add v253, v254, s[44:45] offset:320
	global_atomic_add v253, v254, s[44:45] offset:576
	global_atomic_add v253, v254, s[44:45] offset:832
	global_atomic_add v253, v254, s[44:45] offset:1088
	global_atomic_add v253, v254, s[44:45] offset:1344
	global_atomic_add v253, v254, s[44:45] offset:1600
	global_atomic_add v253, v254, s[44:45] offset:1856
	v_mov_b32_e32 v253, 11264
	global_atomic_add v253, v254, s[44:45] offset:64
	global_atomic_add v253, v254, s[44:45] offset:320
	global_atomic_add v253, v254, s[44:45] offset:576
	global_atomic_add v253, v254, s[44:45] offset:832
	global_atomic_add v253, v254, s[44:45] offset:1088
	global_atomic_add v253, v254, s[44:45] offset:1344
	global_atomic_add v253, v254, s[44:45] offset:1600
	global_atomic_add v253, v254, s[44:45] offset:1856

; __device__ __forceinline__ unsigned xb_ld(unsigned* p)              { return __hip_atomic_load(p, __ATOMIC_RELAXED, __HIP_MEMORY_SCOPE_AGENT); }
; __device__ __forceinline__ unsigned xb_add(unsigned* p, unsigned v) { return __hip_atomic_fetch_add(p, v, __ATOMIC_RELAXED, __HIP_MEMORY_SCOPE_AGENT); }
; #define XB_SPIN(cond, bar) do { unsigned _sp = 0; while (cond) { __builtin_amdgcn_s_sleep(1); \
;     if ((++_sp & 255u) == 0u) { if (xb_ld(&(bar)[XB_TMO])) break; if (_sp > XB_SPIN_CAP) { atomicAdd(&(bar)[XB_TMO], 1u); break; } } } } while (0)
; __device__ __forceinline__ void xcd_barrier(const XcdBarrier& b) {
;   asm volatile("s_waitcnt vmcnt(0)" ::: "memory");
;   __syncthreads();
;   if (threadIdx.x == 0) {
;     unsigned* bar = b.bar;
;     __builtin_amdgcn_s_waitcnt(0);
;     unsigned nloc = b.st[0], nx = b.st[1];
;     if (nloc == 0u) { xcd_barrier_complete(bar, b.x, nloc, nx); b.st[0] = nloc; b.st[1] = nx; }
;     const unsigned old = xb_add(&bar[XB_XSUB(b.x)], 1u);
;     const unsigned gen = old / nloc;
;     if (old + 1u == (gen + 1u) * nloc) {
;       __builtin_amdgcn_fence(__ATOMIC_RELEASE, "agent");
;       asm volatile("s_waitcnt vmcnt(0)" ::: "memory");
;       const unsigned og = xb_add(&bar[XB_TOP], 1u);
;       const unsigned tg = og / nx;
;       if (og + 1u == (tg + 1u) * nx) xb_add(&bar[XB_TOPGEN], 1u);
;       else XB_SPIN(xb_ld(&bar[XB_TOPGEN]) == tg, bar);
;       __builtin_amdgcn_fence(__ATOMIC_ACQUIRE, "agent");
;       xb_add(&bar[XB_XGEN(b.x)], 1u);
.LBB0_677:
	s_or_b64 exec, exec, s[12:13]
	s_waitcnt vmcnt(0)
	s_waitcnt lgkmcnt(0)
	s_barrier
	s_and_saveexec_b64 s[6:7], s[4:5]
	s_cbranch_execz .LBB0_729
	s_waitcnt vmcnt(0) lgkmcnt(0)
	s_add_u32 s98, s98, 1
	s_setprio 3
	v_mov_b32_e32 v253, 0x12810
	ds_read_b32 v254, v253
	ds_read_b32 v253, v253 offset:4
	s_lshl_b32 s101, s33, 8
	s_add_u32 s99, s101, 5120
	s_waitcnt lgkmcnt(0)
	v_readfirstlane_b32 s100, v254
	v_mov_b32_e32 v254, s99
	v_readfirstlane_b32 s99, v253
	s_nop 0
	v_mov_b32_e32 v253, v254
	v_mov_b32_e32 v254, 1
	global_atomic_add v254, v253, v254, s[44:45] offset:64 sc0
	buffer_inv sc1
	s_mul_i32 s100, s100, s98
	s_mul_i32 s99, s99, s98
	s_waitcnt vmcnt(0)
	v_add_u32_e32 v254, 1, v254
	v_cmp_ne_u32_e32 vcc, s100, v254
	s_cbranch_vccnz .Lgb_wait_5
	buffer_wbl2 sc1
	s_waitcnt vmcnt(0)
	v_mov_b32_e32 v254, 1
	v_mov_b32_e32 v253, 9216
	global_atomic_add v253, v254, s[44:45] offset:64
	global_atomic_add v253, v254, s[44:45] offset:320
	global_atomic_add v253, v254, s[44:45] offset:576
	global_atomic_add v253, v254, s[44:45] offset:832
	global_atomic_add v253, v254, s[44:45] offset:1088
	global_atomic_add v253, v254, s[44:45] offset:1344
	global_atomic_add v253, v254, s[44:45] offset:1600
	global_atomic_add v253, v254, s[44:45] offset:1856
	v_mov_b32_e32 v253, 11264
	global_atomic_add v253, v254, s[44:45] offset:64
	global_atomic_add v253, v254, s[44:45] offset:320
	global_atomic_add v253, v254, s[44:45] offset:576
	global_atomic_add v253, v254, s[44:45] offset:832
	global_atomic_add v253, v254, s[44:45] offset:1088
	global_atomic_add v253, v254, s[44:45] offset:1344
	global_atomic_add v253, v254, s[44:45] offset:1600
	global_atomic_add v253, v254, s[44:45] offset:1856

; __device__ __forceinline__ unsigned xb_ld(unsigned* p)              { return __hip_atomic_load(p, __ATOMIC_RELAXED, __HIP_MEMORY_SCOPE_AGENT); }
; __device__ __forceinline__ unsigned xb_add(unsigned* p, unsigned v) { return __hip_atomic_fetch_add(p, v, __ATOMIC_RELAXED, __HIP_MEMORY_SCOPE_AGENT); }
; #define XB_SPIN(cond, bar) do { unsigned _sp = 0; while (cond) { __builtin_amdgcn_s_sleep(1); \
;     if ((++_sp & 255u) == 0u) { if (xb_ld(&(bar)[XB_TMO])) break; if (_sp > XB_SPIN_CAP) { atomicAdd(&(bar)[XB_TMO], 1u); break; } } } } while (0)
; __device__ __forceinline__ void xcd_barrier(const XcdBarrier& b) {
;   asm volatile("s_waitcnt vmcnt(0)" ::: "memory");
;   __syncthreads();
;   if (threadIdx.x == 0) {
;     unsigned* bar = b.bar;
;     __builtin_amdgcn_s_waitcnt(0);
;     unsigned nloc = b.st[0], nx = b.st[1];
;     if (nloc == 0u) { xcd_barrier_complete(bar, b.x, nloc, nx); b.st[0] = nloc; b.st[1] = nx; }
;     const unsigned old = xb_add(&bar[XB_XSUB(b.x)], 1u);
;     const unsigned gen = old / nloc;
;     if (old + 1u == (gen + 1u) * nloc) {
;       __builtin_amdgcn_fence(__ATOMIC_RELEASE, "agent");
;       asm volatile("s_waitcnt vmcnt(0)" ::: "memory");
;       const unsigned og = xb_add(&bar[XB_TOP], 1u);
;       const unsigned tg = og / nx;
;       if (og + 1u == (tg + 1u) * nx) xb_add(&bar[XB_TOPGEN], 1u);
;       else XB_SPIN(xb_ld(&bar[XB_TOPGEN]) == tg, bar);
;       __builtin_amdgcn_fence(__ATOMIC_ACQUIRE, "agent");
;       xb_add(&bar[XB_XGEN(b.x)], 1u);
.LBB0_1015:
	s_or_b64 exec, exec, s[12:13]
	s_waitcnt vmcnt(0)
	s_barrier
	s_and_saveexec_b64 s[12:13], s[4:5]
	s_cbranch_execz .LBB0_1067
	s_waitcnt vmcnt(0) lgkmcnt(0)
	s_add_u32 s98, s98, 1
	s_setprio 3
	v_mov_b32_e32 v253, 0x12810
	ds_read_b32 v254, v253
	ds_read_b32 v253, v253 offset:4
	s_lshl_b32 s101, s33, 8
	s_add_u32 s99, s101, 5120
	s_waitcnt lgkmcnt(0)
	v_readfirstlane_b32 s100, v254
	v_mov_b32_e32 v254, s99
	v_readfirstlane_b32 s99, v253
	s_nop 0
	v_mov_b32_e32 v253, v254
	v_mov_b32_e32 v254, 1
	global_atomic_add v254, v253, v254, s[44:45] offset:64 sc0
	buffer_inv sc1
	s_mul_i32 s100, s100, s98
	s_mul_i32 s99, s99, s98
	s_waitcnt vmcnt(0)
	v_add_u32_e32 v254, 1, v254
	v_cmp_ne_u32_e32 vcc, s100, v254
	s_cbranch_vccnz .Lgb_wait_7
	buffer_wbl2 sc1
	s_waitcnt vmcnt(0)
	v_mov_b32_e32 v254, 1
	v_mov_b32_e32 v253, 9216
	global_atomic_add v253, v254, s[44:45] offset:64
	global_atomic_add v253, v254, s[44:45] offset:320
	global_atomic_add v253, v254, s[44:45] offset:576
	global_atomic_add v253, v254, s[44:45] offset:832
	global_atomic_add v253, v254, s[44:45] offset:1088
	global_atomic_add v253, v254, s[44:45] offset:1344
	global_atomic_add v253, v254, s[44:45] offset:1600
	global_atomic_add v253, v254, s[44:45] offset:1856
	v_mov_b32_e32 v253, 11264
	global_atomic_add v253, v254, s[44:45] offset:64
	global_atomic_add v253, v254, s[44:45] offset:320
	global_atomic_add v253, v254, s[44:45] offset:576
	global_atomic_add v253, v254, s[44:45] offset:832
	global_atomic_add v253, v254, s[44:45] offset:1088
	global_atomic_add v253, v254, s[44:45] offset:1344
	global_atomic_add v253, v254, s[44:45] offset:1600
	global_atomic_add v253, v254, s[44:45] offset:1856

; __device__ __forceinline__ unsigned xb_ld(unsigned* p)              { return __hip_atomic_load(p, __ATOMIC_RELAXED, __HIP_MEMORY_SCOPE_AGENT); }
; __device__ __forceinline__ unsigned xb_add(unsigned* p, unsigned v) { return __hip_atomic_fetch_add(p, v, __ATOMIC_RELAXED, __HIP_MEMORY_SCOPE_AGENT); }
; #define XB_SPIN(cond, bar) do { unsigned _sp = 0; while (cond) { __builtin_amdgcn_s_sleep(1); \
;     if ((++_sp & 255u) == 0u) { if (xb_ld(&(bar)[XB_TMO])) break; if (_sp > XB_SPIN_CAP) { atomicAdd(&(bar)[XB_TMO], 1u); break; } } } } while (0)
; __device__ __forceinline__ void xcd_barrier(const XcdBarrier& b) {
;   asm volatile("s_waitcnt vmcnt(0)" ::: "memory");
;   __syncthreads();
;   if (threadIdx.x == 0) {
;     unsigned* bar = b.bar;
;     __builtin_amdgcn_s_waitcnt(0);
;     unsigned nloc = b.st[0], nx = b.st[1];
;     if (nloc == 0u) { xcd_barrier_complete(bar, b.x, nloc, nx); b.st[0] = nloc; b.st[1] = nx; }
;     const unsigned old = xb_add(&bar[XB_XSUB(b.x)], 1u);
;     const unsigned gen = old / nloc;
;     if (old + 1u == (gen + 1u) * nloc) {
;       __builtin_amdgcn_fence(__ATOMIC_RELEASE, "agent");
;       asm volatile("s_waitcnt vmcnt(0)" ::: "memory");
;       const unsigned og = xb_add(&bar[XB_TOP], 1u);
;       const unsigned tg = og / nx;
;       if (og + 1u == (tg + 1u) * nx) xb_add(&bar[XB_TOPGEN], 1u);
;       else XB_SPIN(xb_ld(&bar[XB_TOPGEN]) == tg, bar);
;       __builtin_amdgcn_fence(__ATOMIC_ACQUIRE, "agent");
;       xb_add(&bar[XB_XGEN(b.x)], 1u);
.Lmy_gbar_8:
	s_add_u32 s98, s98, 1
	s_setprio 3
	v_mov_b32_e32 v253, 0x12810
	ds_read_b32 v254, v253
	ds_read_b32 v253, v253 offset:4
	s_lshl_b32 s101, s33, 8
	s_add_u32 s99, s101, 5120
	s_waitcnt lgkmcnt(0)
	v_readfirstlane_b32 s100, v254
	v_mov_b32_e32 v254, s99
	v_readfirstlane_b32 s99, v253
	s_nop 0
	v_mov_b32_e32 v253, v254
	v_mov_b32_e32 v254, 1
	global_atomic_add v254, v253, v254, s[44:45] offset:64 sc0
	buffer_inv sc1
	s_mul_i32 s100, s100, s98
	s_mul_i32 s99, s99, s98
	s_waitcnt vmcnt(0)
	v_add_u32_e32 v254, 1, v254
	v_cmp_ne_u32_e32 vcc, s100, v254
	s_cbranch_vccnz .Lgb_wait_8
	buffer_wbl2 sc1
	s_waitcnt vmcnt(0)
	v_mov_b32_e32 v254, 1
	v_mov_b32_e32 v253, 9216
	global_atomic_add v253, v254, s[44:45] offset:64
	global_atomic_add v253, v254, s[44:45] offset:320
	global_atomic_add v253, v254, s[44:45] offset:576
	global_atomic_add v253, v254, s[44:45] offset:832
	global_atomic_add v253, v254, s[44:45] offset:1088
	global_atomic_add v253, v254, s[44:45] offset:1344
	global_atomic_add v253, v254, s[44:45] offset:1600
	global_atomic_add v253, v254, s[44:45] offset:1856
	v_mov_b32_e32 v253, 11264
	global_atomic_add v253, v254, s[44:45] offset:64
	global_atomic_add v253, v254, s[44:45] offset:320
	global_atomic_add v253, v254, s[44:45] offset:576
	global_atomic_add v253, v254, s[44:45] offset:832
	global_atomic_add v253, v254, s[44:45] offset:1088
	global_atomic_add v253, v254, s[44:45] offset:1344
	global_atomic_add v253, v254, s[44:45] offset:1600
	global_atomic_add v253, v254, s[44:45] offset:1856

; __device__ __forceinline__ unsigned xb_ld(unsigned* p)              { return __hip_atomic_load(p, __ATOMIC_RELAXED, __HIP_MEMORY_SCOPE_AGENT); }
; __device__ __forceinline__ unsigned xb_add(unsigned* p, unsigned v) { return __hip_atomic_fetch_add(p, v, __ATOMIC_RELAXED, __HIP_MEMORY_SCOPE_AGENT); }
; #define XB_SPIN(cond, bar) do { unsigned _sp = 0; while (cond) { __builtin_amdgcn_s_sleep(1); \
;     if ((++_sp & 255u) == 0u) { if (xb_ld(&(bar)[XB_TMO])) break; if (_sp > XB_SPIN_CAP) { atomicAdd(&(bar)[XB_TMO], 1u); break; } } } } while (0)
; __device__ __forceinline__ void xcd_barrier(const XcdBarrier& b) {
;   asm volatile("s_waitcnt vmcnt(0)" ::: "memory");
;   __syncthreads();
;   if (threadIdx.x == 0) {
;     unsigned* bar = b.bar;
;     __builtin_amdgcn_s_waitcnt(0);
;     unsigned nloc = b.st[0], nx = b.st[1];
;     if (nloc == 0u) { xcd_barrier_complete(bar, b.x, nloc, nx); b.st[0] = nloc; b.st[1] = nx; }
;     const unsigned old = xb_add(&bar[XB_XSUB(b.x)], 1u);
;     const unsigned gen = old / nloc;
;     if (old + 1u == (gen + 1u) * nloc) {
;       __builtin_amdgcn_fence(__ATOMIC_RELEASE, "agent");
;       asm volatile("s_waitcnt vmcnt(0)" ::: "memory");
;       const unsigned og = xb_add(&bar[XB_TOP], 1u);
;       const unsigned tg = og / nx;
;       if (og + 1u == (tg + 1u) * nx) xb_add(&bar[XB_TOPGEN], 1u);
;       else XB_SPIN(xb_ld(&bar[XB_TOPGEN]) == tg, bar);
;       __builtin_amdgcn_fence(__ATOMIC_ACQUIRE, "agent");
;       xb_add(&bar[XB_XGEN(b.x)], 1u);
.LBB0_1196:
	s_waitcnt vmcnt(0)
	s_barrier
	s_and_saveexec_b64 s[2:3], s[4:5]
	s_cbranch_execz .LBB0_1248
	s_waitcnt vmcnt(0) lgkmcnt(0)
	s_add_u32 s98, s98, 1
	s_setprio 3
	v_mov_b32_e32 v253, 0x12810
	ds_read_b32 v254, v253
	ds_read_b32 v253, v253 offset:4
	s_lshl_b32 s101, s33, 8
	s_add_u32 s99, s101, 5120
	s_waitcnt lgkmcnt(0)
	v_readfirstlane_b32 s100, v254
	v_mov_b32_e32 v254, s99
	v_readfirstlane_b32 s99, v253
	s_nop 0
	v_mov_b32_e32 v253, v254
	v_mov_b32_e32 v254, 1
	global_atomic_add v254, v253, v254, s[44:45] offset:64 sc0
	buffer_inv sc1
	s_mul_i32 s100, s100, s98
	s_mul_i32 s99, s99, s98
	s_waitcnt vmcnt(0)
	v_add_u32_e32 v254, 1, v254
	v_cmp_ne_u32_e32 vcc, s100, v254
	s_cbranch_vccnz .Lgb_wait_10
	buffer_wbl2 sc1
	s_waitcnt vmcnt(0)
	v_mov_b32_e32 v254, 1
	v_mov_b32_e32 v253, 9216
	global_atomic_add v253, v254, s[44:45] offset:64
	global_atomic_add v253, v254, s[44:45] offset:320
	global_atomic_add v253, v254, s[44:45] offset:576
	global_atomic_add v253, v254, s[44:45] offset:832
	global_atomic_add v253, v254, s[44:45] offset:1088
	global_atomic_add v253, v254, s[44:45] offset:1344
	global_atomic_add v253, v254, s[44:45] offset:1600
	global_atomic_add v253, v254, s[44:45] offset:1856
	v_mov_b32_e32 v253, 11264
	global_atomic_add v253, v254, s[44:45] offset:64
	global_atomic_add v253, v254, s[44:45] offset:320
	global_atomic_add v253, v254, s[44:45] offset:576
	global_atomic_add v253, v254, s[44:45] offset:832
	global_atomic_add v253, v254, s[44:45] offset:1088
	global_atomic_add v253, v254, s[44:45] offset:1344
	global_atomic_add v253, v254, s[44:45] offset:1600
	global_atomic_add v253, v254, s[44:45] offset:1856

; __device__ __forceinline__ unsigned xb_ld(unsigned* p)              { return __hip_atomic_load(p, __ATOMIC_RELAXED, __HIP_MEMORY_SCOPE_AGENT); }
; __device__ __forceinline__ unsigned xb_add(unsigned* p, unsigned v) { return __hip_atomic_fetch_add(p, v, __ATOMIC_RELAXED, __HIP_MEMORY_SCOPE_AGENT); }
; #define XB_SPIN(cond, bar) do { unsigned _sp = 0; while (cond) { __builtin_amdgcn_s_sleep(1); \
;     if ((++_sp & 255u) == 0u) { if (xb_ld(&(bar)[XB_TMO])) break; if (_sp > XB_SPIN_CAP) { atomicAdd(&(bar)[XB_TMO], 1u); break; } } } } while (0)
; __device__ __forceinline__ void xcd_barrier(const XcdBarrier& b) {
;   asm volatile("s_waitcnt vmcnt(0)" ::: "memory");
;   __syncthreads();
;   if (threadIdx.x == 0) {
;     unsigned* bar = b.bar;
;     __builtin_amdgcn_s_waitcnt(0);
;     unsigned nloc = b.st[0], nx = b.st[1];
;     if (nloc == 0u) { xcd_barrier_complete(bar, b.x, nloc, nx); b.st[0] = nloc; b.st[1] = nx; }
;     const unsigned old = xb_add(&bar[XB_XSUB(b.x)], 1u);
;     const unsigned gen = old / nloc;
;     if (old + 1u == (gen + 1u) * nloc) {
;       __builtin_amdgcn_fence(__ATOMIC_RELEASE, "agent");
;       asm volatile("s_waitcnt vmcnt(0)" ::: "memory");
;       const unsigned og = xb_add(&bar[XB_TOP], 1u);
;       const unsigned tg = og / nx;
;       if (og + 1u == (tg + 1u) * nx) xb_add(&bar[XB_TOPGEN], 1u);
;       else XB_SPIN(xb_ld(&bar[XB_TOPGEN]) == tg, bar);
;       __builtin_amdgcn_fence(__ATOMIC_ACQUIRE, "agent");
;       xb_add(&bar[XB_XGEN(b.x)], 1u);
.LBB0_1327:
	s_or_b64 exec, exec, s[2:3]
	s_waitcnt vmcnt(0)
	s_barrier
	s_and_saveexec_b64 s[2:3], s[4:5]
	s_cbranch_execz .LBB0_1379
	s_waitcnt vmcnt(0) lgkmcnt(0)
	s_add_u32 s98, s98, 1
	s_setprio 3
	v_mov_b32_e32 v253, 0x12810
	ds_read_b32 v254, v253
	ds_read_b32 v253, v253 offset:4
	s_lshl_b32 s101, s33, 8
	s_add_u32 s99, s101, 5120
	s_waitcnt lgkmcnt(0)
	v_readfirstlane_b32 s100, v254
	v_mov_b32_e32 v254, s99
	v_readfirstlane_b32 s99, v253
	s_nop 0
	v_mov_b32_e32 v253, v254
	v_mov_b32_e32 v254, 1
	global_atomic_add v254, v253, v254, s[44:45] offset:64 sc0
	buffer_inv sc1
	s_mul_i32 s100, s100, s98
	s_mul_i32 s99, s99, s98
	s_waitcnt vmcnt(0)
	v_add_u32_e32 v254, 1, v254
	v_cmp_ne_u32_e32 vcc, s100, v254
	s_cbranch_vccnz .Lgb_wait_12
	buffer_wbl2 sc1
	s_waitcnt vmcnt(0)
	v_mov_b32_e32 v254, 1
	v_mov_b32_e32 v253, 9216
	global_atomic_add v253, v254, s[44:45] offset:64
	global_atomic_add v253, v254, s[44:45] offset:320
	global_atomic_add v253, v254, s[44:45] offset:576
	global_atomic_add v253, v254, s[44:45] offset:832
	global_atomic_add v253, v254, s[44:45] offset:1088
	global_atomic_add v253, v254, s[44:45] offset:1344
	global_atomic_add v253, v254, s[44:45] offset:1600
	global_atomic_add v253, v254, s[44:45] offset:1856
	v_mov_b32_e32 v253, 11264
	global_atomic_add v253, v254, s[44:45] offset:64
	global_atomic_add v253, v254, s[44:45] offset:320
	global_atomic_add v253, v254, s[44:45] offset:576
	global_atomic_add v253, v254, s[44:45] offset:832
	global_atomic_add v253, v254, s[44:45] offset:1088
	global_atomic_add v253, v254, s[44:45] offset:1344
	global_atomic_add v253, v254, s[44:45] offset:1600
	global_atomic_add v253, v254, s[44:45] offset:1856
